# P4a Q-GEMM epilogue: hoist 8 row-scale loads, counted vmcnt instead of vmcnt(0) per row group
# speedup vs baseline: 1.0006x; 1.0006x over previous
.LBB0_1003:
	s_lshl_b32 s4, s70, 8
	v_mov_b32_e32 v134, v136
	s_add_i32 s4, s4, s56
	s_nop 0
	v_and_or_b32 v144, v134, 15, s4
	v_ashrrev_i32_e32 v145, 31, v144
	v_lshl_add_u64 v[132:133], v[144:145], 2, s[26:27]
	global_load_dword v204, v[132:133], off
	global_load_dword v205, v[132:133], off offset:64
	global_load_dword v206, v[132:133], off offset:128
	global_load_dword v207, v[132:133], off offset:192
	global_load_dword v208, v[132:133], off offset:512
	global_load_dword v209, v[132:133], off offset:576
	global_load_dword v210, v[132:133], off offset:640
	global_load_dword v211, v[132:133], off offset:704
	v_lshlrev_b64 v[148:149], 11, v[144:145]
	s_lshl_b32 s4, s69, 8
	s_or_b32 s4, s4, s58
	v_and_b32_e32 v134, -16, v134
	v_add_u32_e32 v134, s4, v134
	v_ashrrev_i32_e32 v135, 31, v134
	v_lshl_add_u64 v[148:149], s[24:25], 0, v[148:149]
	v_or_b32_e32 v146, 16, v144
	v_ashrrev_i32_e32 v147, 31, v146
	v_lshl_add_u64 v[152:153], v[146:147], 2, s[26:27]
	s_waitcnt vmcnt(7)
	v_fmamk_f32 v145, v204, 0x3a800000, v143
	v_mul_f32_e32 v150, 0x4b800000, v145
	v_cmp_gt_f32_e32 vcc, s61, v145
	s_nop 1
	v_cndmask_b32_e32 v145, v145, v150, vcc
	v_rsq_f32_e32 v145, v145
	v_lshlrev_b64 v[150:151], 1, v[134:135]
	v_lshl_add_u64 v[134:135], v[148:149], 0, v[150:151]
	v_mul_f32_e32 v148, 0x45800000, v145
	v_cndmask_b32_e32 v145, v145, v148, vcc
	v_mul_f32_e32 v148, 0x3db8aa3b, v145
	v_pk_mul_f32 v[114:115], v[114:115], v[148:149] op_sel_hi:[1,0]
	v_pk_mul_f32 v[112:113], v[112:113], v[148:149] op_sel_hi:[1,0]
	v_pk_mul_f32 v[118:119], v[118:119], v[148:149] op_sel_hi:[1,0]
	v_pk_mul_f32 v[116:117], v[116:117], v[148:149] op_sel_hi:[1,0]
	v_pk_mul_f32 v[122:123], v[122:123], v[148:149] op_sel_hi:[1,0]
	v_pk_mul_f32 v[120:121], v[120:121], v[148:149] op_sel_hi:[1,0]
	v_pk_mul_f32 v[126:127], v[126:127], v[148:149] op_sel_hi:[1,0]
	v_pk_mul_f32 v[124:125], v[124:125], v[148:149] op_sel_hi:[1,0]
	v_cvt_pk_bf16_f32 v112, v112, v113
	v_cvt_pk_bf16_f32 v113, v114, v115
	v_cvt_pk_bf16_f32 v114, v116, v117
	v_cvt_pk_bf16_f32 v115, v118, v119
	v_cvt_pk_bf16_f32 v116, v120, v121
	v_cvt_pk_bf16_f32 v117, v122, v123
	v_cvt_pk_bf16_f32 v118, v124, v125
	v_cvt_pk_bf16_f32 v119, v126, v127
	global_store_dwordx4 v[134:135], v[112:115], off
	global_store_dwordx4 v[134:135], v[116:119], off offset:16
	s_nop 0
	v_lshlrev_b64 v[114:115], 11, v[146:147]
	v_or_b32_e32 v112, 32, v144
	v_lshl_add_u64 v[114:115], s[24:25], 0, v[114:115]
	v_ashrrev_i32_e32 v113, 31, v112
	v_lshl_add_u64 v[114:115], v[114:115], 0, v[150:151]
	s_waitcnt vmcnt(8)
	v_fmamk_f32 v116, v205, 0x3a800000, v143
	v_mul_f32_e32 v117, 0x4b800000, v116
	v_cmp_gt_f32_e32 vcc, s61, v116
	s_nop 1
	v_cndmask_b32_e32 v116, v116, v117, vcc
	v_rsq_f32_e32 v118, v116
	v_lshl_add_u64 v[116:117], v[112:113], 2, s[26:27]
	v_mul_f32_e32 v119, 0x45800000, v118
	v_cndmask_b32_e32 v118, v118, v119, vcc
	v_mul_f32_e32 v118, 0x3db8aa3b, v118
	v_pk_mul_f32 v[98:99], v[98:99], v[118:119] op_sel_hi:[1,0]
	v_pk_mul_f32 v[96:97], v[96:97], v[118:119] op_sel_hi:[1,0]
	v_pk_mul_f32 v[102:103], v[102:103], v[118:119] op_sel_hi:[1,0]
	v_pk_mul_f32 v[100:101], v[100:101], v[118:119] op_sel_hi:[1,0]
	v_pk_mul_f32 v[106:107], v[106:107], v[118:119] op_sel_hi:[1,0]
	v_pk_mul_f32 v[104:105], v[104:105], v[118:119] op_sel_hi:[1,0]
	v_pk_mul_f32 v[110:111], v[110:111], v[118:119] op_sel_hi:[1,0]
	v_pk_mul_f32 v[108:109], v[108:109], v[118:119] op_sel_hi:[1,0]
	v_cvt_pk_bf16_f32 v96, v96, v97
	v_cvt_pk_bf16_f32 v97, v98, v99
	v_cvt_pk_bf16_f32 v98, v100, v101
	v_cvt_pk_bf16_f32 v99, v102, v103
	v_cvt_pk_bf16_f32 v100, v104, v105
	v_cvt_pk_bf16_f32 v101, v106, v107
	v_cvt_pk_bf16_f32 v102, v108, v109
	v_cvt_pk_bf16_f32 v103, v110, v111
	global_store_dwordx4 v[114:115], v[96:99], off
	global_store_dwordx4 v[114:115], v[100:103], off offset:16
	s_nop 0
	v_lshlrev_b64 v[98:99], 11, v[112:113]
	v_or_b32_e32 v96, 48, v144
	v_lshl_add_u64 v[98:99], s[24:25], 0, v[98:99]
	v_ashrrev_i32_e32 v97, 31, v96
	v_lshl_add_u64 v[98:99], v[98:99], 0, v[150:151]
	s_waitcnt vmcnt(9)
	v_fmamk_f32 v100, v206, 0x3a800000, v143
	v_mul_f32_e32 v101, 0x4b800000, v100
	v_cmp_gt_f32_e32 vcc, s61, v100
	s_nop 1
	v_cndmask_b32_e32 v100, v100, v101, vcc
	v_rsq_f32_e32 v102, v100
	v_lshl_add_u64 v[100:101], v[96:97], 2, s[26:27]
	v_mul_f32_e32 v103, 0x45800000, v102
	v_cndmask_b32_e32 v102, v102, v103, vcc
	v_mul_f32_e32 v102, 0x3db8aa3b, v102
	v_pk_mul_f32 v[82:83], v[82:83], v[102:103] op_sel_hi:[1,0]
	v_pk_mul_f32 v[80:81], v[80:81], v[102:103] op_sel_hi:[1,0]
	v_pk_mul_f32 v[86:87], v[86:87], v[102:103] op_sel_hi:[1,0]
	v_pk_mul_f32 v[84:85], v[84:85], v[102:103] op_sel_hi:[1,0]
	v_pk_mul_f32 v[90:91], v[90:91], v[102:103] op_sel_hi:[1,0]
	v_pk_mul_f32 v[88:89], v[88:89], v[102:103] op_sel_hi:[1,0]
	v_pk_mul_f32 v[94:95], v[94:95], v[102:103] op_sel_hi:[1,0]
	v_pk_mul_f32 v[92:93], v[92:93], v[102:103] op_sel_hi:[1,0]
	v_cvt_pk_bf16_f32 v80, v80, v81
	v_cvt_pk_bf16_f32 v81, v82, v83
	v_cvt_pk_bf16_f32 v82, v84, v85
	v_cvt_pk_bf16_f32 v83, v86, v87
	v_cvt_pk_bf16_f32 v84, v88, v89
	v_cvt_pk_bf16_f32 v85, v90, v91
	v_cvt_pk_bf16_f32 v86, v92, v93
	v_cvt_pk_bf16_f32 v87, v94, v95
	global_store_dwordx4 v[98:99], v[80:83], off
	global_store_dwordx4 v[98:99], v[84:87], off offset:16
	s_nop 0
	s_waitcnt vmcnt(10)
	v_fmamk_f32 v80, v207, 0x3a800000, v143
	v_mul_f32_e32 v81, 0x4b800000, v80
	v_cmp_gt_f32_e32 vcc, s61, v80
	s_nop 1
	v_cndmask_b32_e32 v80, v80, v81, vcc
	v_rsq_f32_e32 v82, v80
	v_lshlrev_b64 v[80:81], 11, v[96:97]
	v_lshl_add_u64 v[80:81], s[24:25], 0, v[80:81]
	v_lshl_add_u64 v[80:81], v[80:81], 0, v[150:151]
	v_mul_f32_e32 v83, 0x45800000, v82
	v_cndmask_b32_e32 v82, v82, v83, vcc
	v_mul_f32_e32 v82, 0x3db8aa3b, v82
	v_pk_mul_f32 v[70:71], v[70:71], v[82:83] op_sel_hi:[1,0]
	v_pk_mul_f32 v[68:69], v[68:69], v[82:83] op_sel_hi:[1,0]
	v_pk_mul_f32 v[84:85], v[66:67], v[82:83] op_sel_hi:[1,0]
	v_pk_mul_f32 v[66:67], v[64:65], v[82:83] op_sel_hi:[1,0]
	v_pk_mul_f32 v[78:79], v[78:79], v[82:83] op_sel_hi:[1,0]
	v_pk_mul_f32 v[76:77], v[76:77], v[82:83] op_sel_hi:[1,0]
	v_pk_mul_f32 v[74:75], v[74:75], v[82:83] op_sel_hi:[1,0]
	v_pk_mul_f32 v[72:73], v[72:73], v[82:83] op_sel_hi:[1,0]
	v_cvt_pk_bf16_f32 v64, v68, v69
	v_cvt_pk_bf16_f32 v65, v70, v71
	v_cvt_pk_bf16_f32 v66, v66, v67
	v_cvt_pk_bf16_f32 v67, v84, v85
	v_cvt_pk_bf16_f32 v68, v76, v77
	v_cvt_pk_bf16_f32 v69, v78, v79
	v_cvt_pk_bf16_f32 v70, v72, v73
	v_cvt_pk_bf16_f32 v71, v74, v75
	global_store_dwordx4 v[80:81], v[64:67], off
	global_store_dwordx4 v[80:81], v[68:71], off offset:16
	s_nop 0
	v_lshl_add_u64 v[64:65], v[134:135], 0, s[28:29]
	s_waitcnt vmcnt(11)
	v_fmamk_f32 v66, v208, 0x3a800000, v143
	v_mul_f32_e32 v67, 0x4b800000, v66
	v_cmp_gt_f32_e32 vcc, s61, v66
	s_nop 1
	v_cndmask_b32_e32 v66, v66, v67, vcc
	v_rsq_f32_e32 v68, v66
	v_add_co_u32_e64 v66, s[4:5], s43, v134
	v_mul_f32_e32 v69, 0x45800000, v68
	v_cndmask_b32_e32 v68, v68, v69, vcc
	v_mul_f32_e32 v68, 0x3db8aa3b, v68
	v_pk_mul_f32 v[50:51], v[50:51], v[68:69] op_sel_hi:[1,0]
	v_pk_mul_f32 v[48:49], v[48:49], v[68:69] op_sel_hi:[1,0]
	v_pk_mul_f32 v[54:55], v[54:55], v[68:69] op_sel_hi:[1,0]
	v_pk_mul_f32 v[52:53], v[52:53], v[68:69] op_sel_hi:[1,0]
	v_addc_co_u32_e64 v67, s[4:5], 0, v135, s[4:5]
	v_pk_mul_f32 v[62:63], v[62:63], v[68:69] op_sel_hi:[1,0]
	v_pk_mul_f32 v[60:61], v[60:61], v[68:69] op_sel_hi:[1,0]
	v_pk_mul_f32 v[58:59], v[58:59], v[68:69] op_sel_hi:[1,0]
	v_pk_mul_f32 v[56:57], v[56:57], v[68:69] op_sel_hi:[1,0]
	v_cvt_pk_bf16_f32 v48, v48, v49
	v_cvt_pk_bf16_f32 v49, v50, v51
	v_cvt_pk_bf16_f32 v50, v52, v53
	v_cvt_pk_bf16_f32 v51, v54, v55
	v_cvt_pk_bf16_f32 v52, v60, v61
	v_cvt_pk_bf16_f32 v53, v62, v63
	v_cvt_pk_bf16_f32 v54, v56, v57
	v_cvt_pk_bf16_f32 v55, v58, v59
	global_store_dwordx4 v[66:67], v[48:51], off
	global_store_dwordx4 v[64:65], v[52:55], off offset:16
	s_nop 0
	v_lshl_add_u64 v[48:49], v[134:135], 0, s[48:49]
	s_waitcnt vmcnt(12)
	v_fmamk_f32 v50, v209, 0x3a800000, v143
	v_mul_f32_e32 v51, 0x4b800000, v50
	v_cmp_gt_f32_e32 vcc, s61, v50
	s_nop 1
	v_cndmask_b32_e32 v50, v50, v51, vcc
	v_rsq_f32_e32 v52, v50
	v_add_co_u32_e64 v50, s[4:5], s62, v134
	v_mul_f32_e32 v53, 0x45800000, v52
	v_cndmask_b32_e32 v52, v52, v53, vcc
	v_mul_f32_e32 v52, 0x3db8aa3b, v52
	v_pk_mul_f32 v[34:35], v[34:35], v[52:53] op_sel_hi:[1,0]
	v_pk_mul_f32 v[32:33], v[32:33], v[52:53] op_sel_hi:[1,0]
	v_pk_mul_f32 v[38:39], v[38:39], v[52:53] op_sel_hi:[1,0]
	v_pk_mul_f32 v[36:37], v[36:37], v[52:53] op_sel_hi:[1,0]
	v_addc_co_u32_e64 v51, s[4:5], 0, v135, s[4:5]
	v_pk_mul_f32 v[46:47], v[46:47], v[52:53] op_sel_hi:[1,0]
	v_pk_mul_f32 v[44:45], v[44:45], v[52:53] op_sel_hi:[1,0]
	v_pk_mul_f32 v[42:43], v[42:43], v[52:53] op_sel_hi:[1,0]
	v_pk_mul_f32 v[40:41], v[40:41], v[52:53] op_sel_hi:[1,0]
	v_cvt_pk_bf16_f32 v32, v32, v33
	v_cvt_pk_bf16_f32 v33, v34, v35
	v_cvt_pk_bf16_f32 v34, v36, v37
	v_cvt_pk_bf16_f32 v35, v38, v39
	v_cvt_pk_bf16_f32 v36, v44, v45
	v_cvt_pk_bf16_f32 v37, v46, v47
	v_cvt_pk_bf16_f32 v38, v40, v41
	v_cvt_pk_bf16_f32 v39, v42, v43
	global_store_dwordx4 v[50:51], v[32:35], off
	global_store_dwordx4 v[48:49], v[36:39], off offset:16
	s_nop 0
	v_lshl_add_u64 v[32:33], v[134:135], 0, s[50:51]
	s_waitcnt vmcnt(13)
	v_fmamk_f32 v34, v210, 0x3a800000, v143
	v_mul_f32_e32 v35, 0x4b800000, v34
	v_cmp_gt_f32_e32 vcc, s61, v34
	s_nop 1
	v_cndmask_b32_e32 v34, v34, v35, vcc
	v_rsq_f32_e32 v36, v34
	v_add_co_u32_e64 v34, s[4:5], s63, v134
	v_mul_f32_e32 v37, 0x45800000, v36
	v_cndmask_b32_e32 v36, v36, v37, vcc
	v_mul_f32_e32 v36, 0x3db8aa3b, v36
	v_pk_mul_f32 v[18:19], v[18:19], v[36:37] op_sel_hi:[1,0]
	v_pk_mul_f32 v[16:17], v[16:17], v[36:37] op_sel_hi:[1,0]
	v_pk_mul_f32 v[22:23], v[22:23], v[36:37] op_sel_hi:[1,0]
	v_pk_mul_f32 v[20:21], v[20:21], v[36:37] op_sel_hi:[1,0]
	v_addc_co_u32_e64 v35, s[4:5], 0, v135, s[4:5]
	v_pk_mul_f32 v[30:31], v[30:31], v[36:37] op_sel_hi:[1,0]
	v_pk_mul_f32 v[28:29], v[28:29], v[36:37] op_sel_hi:[1,0]
	v_pk_mul_f32 v[26:27], v[26:27], v[36:37] op_sel_hi:[1,0]
	v_pk_mul_f32 v[24:25], v[24:25], v[36:37] op_sel_hi:[1,0]
	v_cvt_pk_bf16_f32 v16, v16, v17
	v_cvt_pk_bf16_f32 v17, v18, v19
	v_cvt_pk_bf16_f32 v18, v20, v21
	v_cvt_pk_bf16_f32 v19, v22, v23
	v_cvt_pk_bf16_f32 v20, v28, v29
	v_cvt_pk_bf16_f32 v21, v30, v31
	v_cvt_pk_bf16_f32 v22, v24, v25
	v_cvt_pk_bf16_f32 v23, v26, v27
	global_store_dwordx4 v[34:35], v[16:19], off
	global_store_dwordx4 v[32:33], v[20:23], off offset:16
	s_nop 0
	s_andn2_b64 vcc, exec, s[2:3]
	v_lshl_add_u64 v[16:17], v[134:135], 0, s[52:53]
	s_waitcnt vmcnt(14)
	v_fmamk_f32 v18, v211, 0x3a800000, v143
	v_mul_f32_e32 v19, 0x4b800000, v18
	v_cmp_gt_f32_e64 s[2:3], s61, v18
	s_nop 1
	v_cndmask_b32_e64 v18, v18, v19, s[2:3]
	v_rsq_f32_e32 v20, v18
	v_add_co_u32_e64 v18, s[4:5], s64, v134
	v_mul_f32_e32 v21, 0x45800000, v20
	v_cndmask_b32_e64 v20, v20, v21, s[2:3]
	v_mul_f32_e32 v20, 0x3db8aa3b, v20
	v_pk_mul_f32 v[2:3], v[2:3], v[20:21] op_sel_hi:[1,0]
	v_pk_mul_f32 v[0:1], v[0:1], v[20:21] op_sel_hi:[1,0]
	v_pk_mul_f32 v[6:7], v[6:7], v[20:21] op_sel_hi:[1,0]
	v_pk_mul_f32 v[4:5], v[4:5], v[20:21] op_sel_hi:[1,0]
	v_pk_mul_f32 v[14:15], v[14:15], v[20:21] op_sel_hi:[1,0]
	v_pk_mul_f32 v[12:13], v[12:13], v[20:21] op_sel_hi:[1,0]
	v_pk_mul_f32 v[10:11], v[10:11], v[20:21] op_sel_hi:[1,0]
	v_pk_mul_f32 v[8:9], v[8:9], v[20:21] op_sel_hi:[1,0]
	v_addc_co_u32_e64 v19, s[4:5], 0, v135, s[4:5]
	v_cvt_pk_bf16_f32 v0, v0, v1
	v_cvt_pk_bf16_f32 v1, v2, v3
	v_cvt_pk_bf16_f32 v2, v4, v5
	v_cvt_pk_bf16_f32 v3, v6, v7
	v_cvt_pk_bf16_f32 v4, v12, v13
	v_cvt_pk_bf16_f32 v5, v14, v15
	v_cvt_pk_bf16_f32 v6, v8, v9
	v_cvt_pk_bf16_f32 v7, v10, v11
	s_mov_b64 s[2:3], -1
	global_store_dwordx4 v[18:19], v[0:3], off
	global_store_dwordx4 v[16:17], v[4:7], off offset:16
	s_cbranch_vccnz .LBB0_992
	v_mov_b32_e32 v8, 0
	s_andn2_b64 vcc, exec, s[22:23]
	s_nop 0
	v_mfma_f32_4x4x1_16b_f32 v[112:115], v8, v8, 0
	s_nop 0
	v_mfma_f32_4x4x1_16b_f32 v[116:119], v8, v8, 0
	s_nop 0
	v_mfma_f32_4x4x1_16b_f32 v[96:99], v8, v8, 0
	s_nop 0
	v_mfma_f32_4x4x1_16b_f32 v[100:103], v8, v8, 0
	s_nop 0
	v_mfma_f32_4x4x1_16b_f32 v[80:83], v8, v8, 0
	s_nop 0
	v_mfma_f32_4x4x1_16b_f32 v[84:87], v8, v8, 0
	s_nop 0
	v_mfma_f32_4x4x1_16b_f32 v[68:71], v8, v8, 0
	s_nop 0
	v_mfma_f32_4x4x1_16b_f32 v[64:67], v8, v8, 0
	s_nop 0
	v_mfma_f32_4x4x1_16b_f32 v[120:123], v8, v8, 0
	s_nop 0
	v_mfma_f32_4x4x1_16b_f32 v[124:127], v8, v8, 0
	s_nop 0
	v_mfma_f32_4x4x1_16b_f32 v[104:107], v8, v8, 0
	s_nop 0
	v_mfma_f32_4x4x1_16b_f32 v[108:111], v8, v8, 0
	s_nop 0
	v_mfma_f32_4x4x1_16b_f32 v[88:91], v8, v8, 0
	s_nop 0
	v_mfma_f32_4x4x1_16b_f32 v[92:95], v8, v8, 0
	s_nop 0
	v_mfma_f32_4x4x1_16b_f32 v[76:79], v8, v8, 0
	s_nop 0
	v_mfma_f32_4x4x1_16b_f32 v[72:75], v8, v8, 0
	s_nop 0
	v_mfma_f32_4x4x1_16b_f32 v[48:51], v8, v8, 0
	s_nop 0
	v_mfma_f32_4x4x1_16b_f32 v[52:55], v8, v8, 0
	s_nop 0
	v_mfma_f32_4x4x1_16b_f32 v[32:35], v8, v8, 0
	s_nop 0
	v_mfma_f32_4x4x1_16b_f32 v[36:39], v8, v8, 0
	s_nop 0
	v_mfma_f32_4x4x1_16b_f32 v[16:19], v8, v8, 0
	s_nop 0
	v_mfma_f32_4x4x1_16b_f32 v[20:23], v8, v8, 0
	s_nop 0
	v_mfma_f32_4x4x1_16b_f32 v[0:3], v8, v8, 0
	s_nop 0
	v_mfma_f32_4x4x1_16b_f32 v[4:7], v8, v8, 0
	s_nop 0
	v_mfma_f32_4x4x1_16b_f32 v[60:63], v8, v8, 0
	s_nop 0
	v_mfma_f32_4x4x1_16b_f32 v[56:59], v8, v8, 0
	s_nop 0
	v_mfma_f32_4x4x1_16b_f32 v[44:47], v8, v8, 0
	s_nop 0
	v_mfma_f32_4x4x1_16b_f32 v[40:43], v8, v8, 0
	s_nop 0
	v_mfma_f32_4x4x1_16b_f32 v[28:31], v8, v8, 0
	s_nop 0
	v_mfma_f32_4x4x1_16b_f32 v[24:27], v8, v8, 0
	s_nop 0
	v_mfma_f32_4x4x1_16b_f32 v[12:15], v8, v8, 0
	s_nop 0
	v_mfma_f32_4x4x1_16b_f32 v[8:11], v8, v8, 0
	s_cbranch_vccnz .LBB0_991
	s_barrier
	s_branch .LBB0_991
